# add P12 epilogue bias/row weights via LDS-DMA (opt10) on top of v76
# baseline (speedup 1.0000x reference)
;     __device__ __forceinline__ void operator()(const f32x4 (&acc)[2][2][4][2], const Unit& u, int wr, int wc, int fr, int fq) const {
;     ...
;         const float* bb = bias + (size_t)u.e * ldc + col0;
;         f32x4 bv[2][2];
; #pragma unroll
;         for (int bj = 0; bj < 2; ++bj)
; #pragma unroll
;             for (int n = 0; n < 2; ++n) bv[bj][n] = *(const f32x4*)(bb + bj * HALF + 4 * n);
;         float wq[2][4];
; #pragma unroll
;         for (int ai = 0; ai < 2; ++ai)
; #pragma unroll
;             for (int m = 0; m < 4; ++m) wq[ai][m] = sw[row0 + ai * HALF + m * 16];
; template <class Epi, class Sched, bool ALIGN_EPI = false, bool SP2 = false, bool GATHER = false, bool F8 = false>
; __device__ __forceinline__ void gemm_phase(PG8_LAS unsigned char* lds, const Gemm g, const Sched& S, const Epi& E) {
;     ...
; #pragma unroll
;         for (int a = 0; a < 2; ++a)
; #pragma unroll
;             for (int b = 0; b < 2; ++b)
; #pragma unroll
;                 for (int m = 0; m < 4; ++m)
; #pragma unroll
;                     for (int n = 0; n < 2; ++n) acc[a][b][m][n] = (f32x4){0.f, 0.f, 0.f, 0.f}; }
;         cur = nxt; cA = nA; cB = nB; ++ui;
.LBB0_1564:
	s_lshl_b64 s[42:43], s[38:39], 19
	s_add_u32 s42, s20, s42
	s_addc_u32 s43, s21, s43
	s_and_b64 s[52:53], exec, s[0:1]
	s_cselect_b32 s39, s43, s61
	s_cselect_b32 s75, s42, s60
	s_ashr_i32 s41, s40, 31
	s_lshl_b64 s[52:53], s[40:41], 22
	s_add_u32 s41, s24, s52
	s_addc_u32 s62, s25, s53
	s_ashr_i32 s37, s36, 31
	s_lshl_b64 s[52:53], s[36:37], 19
	s_add_u32 s52, s41, s52
	s_addc_u32 s53, s62, s53
	s_and_b64 s[62:63], exec, s[0:1]
	s_cselect_b32 s37, s53, s59
	s_cselect_b32 s41, s52, s58
	s_add_u32 s76, s58, 0x100
	v_mov_b32_e32 v32, 0
	s_addc_u32 s77, s59, 0
	s_mov_b32 s78, -2
	v_mov_b32_e32 v33, v32
	v_mov_b32_e32 v34, v32
	v_mov_b32_e32 v35, v32
	v_mov_b32_e32 v36, v32
	v_mov_b32_e32 v37, v32
	v_mov_b32_e32 v38, v32
	v_mov_b32_e32 v39, v32
	v_mov_b32_e32 v48, v32
	v_mov_b32_e32 v49, v32
	v_mov_b32_e32 v50, v32
	v_mov_b32_e32 v51, v32
	v_mov_b32_e32 v52, v32
	v_mov_b32_e32 v53, v32
	v_mov_b32_e32 v54, v32
	v_mov_b32_e32 v55, v32
	v_mov_b32_e32 v64, v32
	v_mov_b32_e32 v65, v32
	v_mov_b32_e32 v66, v32
	v_mov_b32_e32 v67, v32
	v_mov_b32_e32 v68, v32
	v_mov_b32_e32 v69, v32
	v_mov_b32_e32 v70, v32
	v_mov_b32_e32 v71, v32
	v_mov_b32_e32 v80, v32
	v_mov_b32_e32 v81, v32
	v_mov_b32_e32 v82, v32
	v_mov_b32_e32 v83, v32
	v_mov_b32_e32 v84, v32
	v_mov_b32_e32 v85, v32
	v_mov_b32_e32 v86, v32
	v_mov_b32_e32 v87, v32
	v_mov_b32_e32 v40, v32
	v_mov_b32_e32 v41, v32
	v_mov_b32_e32 v42, v32
	v_mov_b32_e32 v43, v32
	v_mov_b32_e32 v44, v32
	v_mov_b32_e32 v45, v32
	v_mov_b32_e32 v46, v32
	v_mov_b32_e32 v47, v32
	v_mov_b32_e32 v56, v32
	v_mov_b32_e32 v57, v32
	v_mov_b32_e32 v58, v32
	v_mov_b32_e32 v59, v32
	v_mov_b32_e32 v60, v32
	v_mov_b32_e32 v61, v32
	v_mov_b32_e32 v62, v32
	v_mov_b32_e32 v63, v32
	v_mov_b32_e32 v72, v32
	v_mov_b32_e32 v73, v32
	v_mov_b32_e32 v74, v32
	v_mov_b32_e32 v75, v32
	v_mov_b32_e32 v76, v32
	v_mov_b32_e32 v77, v32
	v_mov_b32_e32 v78, v32
	v_mov_b32_e32 v79, v32
	v_mov_b32_e32 v88, v32
	v_mov_b32_e32 v89, v32
	v_mov_b32_e32 v90, v32
	v_mov_b32_e32 v91, v32
	v_mov_b32_e32 v92, v32
	v_mov_b32_e32 v93, v32
	v_mov_b32_e32 v94, v32
	v_mov_b32_e32 v95, v32
	v_mov_b32_e32 v96, v32
	v_mov_b32_e32 v97, v32
	v_mov_b32_e32 v98, v32
	v_mov_b32_e32 v99, v32
	v_mov_b32_e32 v100, v32
	v_mov_b32_e32 v101, v32
	v_mov_b32_e32 v102, v32
	v_mov_b32_e32 v103, v32
	v_mov_b32_e32 v112, v32
	v_mov_b32_e32 v113, v32
	v_mov_b32_e32 v114, v32
	v_mov_b32_e32 v115, v32
	v_mov_b32_e32 v116, v32
	v_mov_b32_e32 v117, v32
	v_mov_b32_e32 v118, v32
	v_mov_b32_e32 v119, v32
	v_mov_b32_e32 v128, v32
	v_mov_b32_e32 v129, v32
	v_mov_b32_e32 v130, v32
	v_mov_b32_e32 v131, v32
	v_mov_b32_e32 v132, v32
	v_mov_b32_e32 v133, v32
	v_mov_b32_e32 v134, v32
	v_mov_b32_e32 v135, v32
	v_mov_b32_e32 v136, v32
	v_mov_b32_e32 v137, v32
	v_mov_b32_e32 v138, v32
	v_mov_b32_e32 v139, v32
	v_mov_b32_e32 v140, v32
	v_mov_b32_e32 v141, v32
	v_mov_b32_e32 v142, v32
	v_mov_b32_e32 v143, v32
	v_mov_b32_e32 v104, v32
	v_mov_b32_e32 v105, v32
	v_mov_b32_e32 v106, v32
	v_mov_b32_e32 v107, v32
	v_mov_b32_e32 v108, v32
	v_mov_b32_e32 v109, v32
	v_mov_b32_e32 v110, v32
	v_mov_b32_e32 v111, v32
	v_mov_b32_e32 v120, v32
	v_mov_b32_e32 v121, v32
	v_mov_b32_e32 v122, v32
	v_mov_b32_e32 v123, v32
	v_mov_b32_e32 v124, v32
	v_mov_b32_e32 v125, v32
	v_mov_b32_e32 v126, v32
	v_mov_b32_e32 v127, v32
	v_mov_b32_e32 v144, v32
	v_mov_b32_e32 v145, v32
	v_mov_b32_e32 v146, v32
	v_mov_b32_e32 v147, v32
	v_mov_b32_e32 v148, v32
	v_mov_b32_e32 v149, v32
	v_mov_b32_e32 v150, v32
	v_mov_b32_e32 v151, v32
	v_mov_b32_e32 v152, v32
	v_mov_b32_e32 v153, v32
	v_mov_b32_e32 v154, v32
	v_mov_b32_e32 v155, v32
	v_mov_b32_e32 v156, v32
	v_mov_b32_e32 v157, v32
	v_mov_b32_e32 v158, v32
	v_mov_b32_e32 v159, v32
	v_lshrrev_b32_e32 v228, 4, v184
	v_bfe_u32 v229, v186, 5, 2
	v_add_u32_e32 v228, v228, v229
	v_lshlrev_b32_e32 v228, 10, v228
	v_add_u32_e32 v228, 0x21000, v228
	v_and_b32_e32 v230, 31, v224
	v_and_b32_e32 v231, 0x60, v186
	v_add_u32_e32 v230, v230, v231
	v_and_b32_e32 v231, 32, v224
	v_lshl_add_u32 v230, v231, 2, v230
	v_lshl_add_u32 v230, s56, 8, v230
	v_lshlrev_b32_e32 v230, 2, v230
	v_lshl_add_u32 v230, v174, 13, v230
	v_mov_b32_e32 v231, 0
	v_lshl_add_u64 v[232:233], s[44:45], 0, v[230:231]
	v_readfirstlane_b32 s100, v228
	s_mov_b32 m0, s100
	s_nop 0
	global_load_lds_dword v[232:233], off
	v_and_b32_e32 v230, 0x40, v184
	v_add_u32_e32 v230, v230, v224
	v_lshl_add_u32 v230, s54, 8, v230
	v_lshlrev_b32_e32 v230, 2, v230
	v_lshl_add_u64 v[232:233], s[10:11], 0, v[230:231]
	s_add_i32 m0, s100, 0x100
	s_nop 0
	global_load_lds_dword v[232:233], off
	v_mov_b32_e32 v230, 0x200
	v_lshl_add_u64 v[232:233], v[232:233], 0, v[230:231]
	s_add_i32 m0, s100, 0x200
	s_nop 0
	global_load_lds_dword v[232:233], off

;     __device__ __forceinline__ void operator()(const f32x4 (&acc)[2][2][4][2], const Unit& u, int wr, int wc, int fr, int fq) const {
;         const int row0 = u.pm * BM + wr * 64 + fr, col0 = u.pn * BM + wc * 32 + 8 * fq;
;         const float* bb = bias + (size_t)u.e * ldc + col0;
;         f32x4 bv[2][2];
; #pragma unroll
;         for (int bj = 0; bj < 2; ++bj)
; #pragma unroll
;             for (int n = 0; n < 2; ++n) bv[bj][n] = *(const f32x4*)(bb + bj * HALF + 4 * n);
;         float wq[2][4];
; #pragma unroll
;         for (int ai = 0; ai < 2; ++ai)
; #pragma unroll
;             for (int m = 0; m < 4; ++m) wq[ai][m] = sw[row0 + ai * HALF + m * 16];
;         asm volatile("s_waitcnt vmcnt(0)" ::: "memory");
; #pragma unroll
;         for (int ai = 0; ai < 2; ++ai)
; #pragma unroll
;             for (int m = 0; m < 4; ++m) { const int r = row0 + ai * HALF + m * 16; const float w8 = wq[ai][m] * oscale; unsigned char* rowp = O + (size_t)r * ldc + col0;
; #pragma unroll
;                 for (int bj = 0; bj < 2; ++bj) { f32x4 v0 = (acc[ai][bj][m][0] * ascale + bv[bj][0]) * w8, v1 = (acc[ai][bj][m][1] * ascale + bv[bj][1]) * w8;
; #pragma unroll
;                     for (int j = 0; j < 4; ++j) { v0[j] = __builtin_amdgcn_fmed3f(v0[j], -448.0f, 448.0f); v1[j] = __builtin_amdgcn_fmed3f(v1[j], -448.0f, 448.0f); }
;                     int w0 = 0, w1 = 0;
;                     w0 = __builtin_amdgcn_cvt_pk_fp8_f32(v0[0], v0[1], w0, false); w0 = __builtin_amdgcn_cvt_pk_fp8_f32(v0[2], v0[3], w0, true);
;                     w1 = __builtin_amdgcn_cvt_pk_fp8_f32(v1[0], v1[1], w1, false); w1 = __builtin_amdgcn_cvt_pk_fp8_f32(v1[2], v1[3], w1, true);
;                     u32x2 w; w.x = (unsigned)w0; w.y = (unsigned)w1; *(u32x2*)(rowp + bj * HALF) = w; } }
.LBB0_1568:
	v_lshl_or_b32 v18, s56, 8, v186
	v_lshl_add_u32 v16, s54, 8, v184
	v_lshrrev_b32_e32 v0, 4, v184
	v_bfe_u32 v1, v186, 5, 2
	v_add_u32_e32 v0, v0, v1
	v_lshlrev_b32_e32 v0, 10, v0
	v_add_u32_e32 v0, 0x21000, v0
	v_and_b32_e32 v1, 15, v184
	v_lshl_add_u32 v1, v1, 2, v0
	v_and_b32_e32 v20, 31, v186
	v_lshl_add_u32 v0, v20, 2, v0
	ds_read_b32 v178, v1 offset:256
	ds_read_b128 v[12:15], v0
	ds_read_b128 v[8:11], v0 offset:16
	ds_read_b128 v[4:7], v0 offset:128
	ds_read_b32 v179, v1 offset:320
	ds_read_b32 v180, v1 offset:512
	ds_read_b32 v181, v1 offset:576
	ds_read_b32 v182, v1 offset:640
	ds_read_b32 v175, v1 offset:384
	ds_read_b32 v177, v1 offset:448
	ds_read_b32 v20, v1 offset:704
	ds_read_b128 v[0:3], v0 offset:144
	v_ashrrev_i32_e32 v19, 31, v18
	v_ashrrev_i32_e32 v17, 31, v16
	v_or_b32_e32 v22, 16, v16
	v_or_b32_e32 v28, 32, v16
	v_or_b32_e32 v30, 48, v16
	v_ashrrev_i32_e32 v23, 31, v22
	v_ashrrev_i32_e32 v29, 31, v28
	v_ashrrev_i32_e32 v31, 31, v30
	v_mov_b32_e32 v24, 0
	v_mov_b32_e32 v25, 0
	v_mov_b32_e32 v26, 0
	v_mov_b32_e32 v27, 0
	v_lshlrev_b64 v[16:17], 11, v[16:17]
	v_lshl_add_u64 v[16:17], s[8:9], 0, v[16:17]
	v_lshl_add_u64 v[16:17], v[16:17], 0, v[18:19]
	v_lshlrev_b64 v[22:23], 11, v[22:23]
	v_lshl_add_u64 v[22:23], s[8:9], 0, v[22:23]
	v_lshl_add_u64 v[22:23], v[22:23], 0, v[18:19]
	v_readlane_b32 s37, v253, 2
	s_waitcnt lgkmcnt(0)
	v_mul_f32_e32 v174, 0x42800000, v178
	v_pk_fma_f32 v[156:157], v[156:157], s[16:17], v[12:13] op_sel_hi:[1,0,1]
	v_pk_fma_f32 v[152:153], v[152:153], s[16:17], v[8:9] op_sel_hi:[1,0,1]
	v_pk_fma_f32 v[136:137], v[136:137], s[16:17], v[0:1] op_sel_hi:[1,0,1]
	v_pk_fma_f32 v[140:141], v[140:141], s[16:17], v[4:5] op_sel_hi:[1,0,1]
	v_pk_fma_f32 v[158:159], v[158:159], s[16:17], v[14:15] op_sel_hi:[1,0,1]
	v_pk_fma_f32 v[154:155], v[154:155], s[16:17], v[10:11] op_sel_hi:[1,0,1]
	v_pk_fma_f32 v[142:143], v[142:143], s[16:17], v[6:7] op_sel_hi:[1,0,1]
	v_pk_fma_f32 v[138:139], v[138:139], s[16:17], v[2:3] op_sel_hi:[1,0,1]
	v_pk_fma_f32 v[148:149], v[148:149], s[16:17], v[12:13] op_sel_hi:[1,0,1]
	v_pk_mul_f32 v[156:157], v[156:157], v[174:175] op_sel_hi:[1,0]
	v_pk_mul_f32 v[152:153], v[152:153], v[174:175] op_sel_hi:[1,0]
	v_pk_mul_f32 v[140:141], v[140:141], v[174:175] op_sel_hi:[1,0]
	v_pk_mul_f32 v[136:137], v[136:137], v[174:175] op_sel_hi:[1,0]
	v_med3_f32 v21, v156, s70, v191
	v_med3_f32 v152, v152, s70, v191
	v_med3_f32 v156, v157, s70, v191
	v_med3_f32 v153, v153, s70, v191
	v_med3_f32 v140, v140, s70, v191
	v_med3_f32 v136, v136, s70, v191
	v_med3_f32 v141, v141, s70, v191
	v_med3_f32 v137, v137, s70, v191
	v_cvt_pk_fp8_f32 v24, v21, v156
	v_cvt_pk_fp8_f32 v25, v152, v153
	v_cvt_pk_fp8_f32 v26, v140, v141
	v_cvt_pk_fp8_f32 v27, v136, v137
	v_pk_mul_f32 v[158:159], v[158:159], v[174:175] op_sel_hi:[1,0]
	v_pk_mul_f32 v[154:155], v[154:155], v[174:175] op_sel_hi:[1,0]
	v_pk_mul_f32 v[142:143], v[142:143], v[174:175] op_sel_hi:[1,0]
	v_pk_mul_f32 v[138:139], v[138:139], v[174:175] op_sel_hi:[1,0]
	v_med3_f32 v157, v158, s70, v191
	v_med3_f32 v154, v154, s70, v191
	v_med3_f32 v158, v159, s70, v191
	v_med3_f32 v155, v155, s70, v191
	v_med3_f32 v142, v142, s70, v191
	v_med3_f32 v138, v138, s70, v191
	v_med3_f32 v143, v143, s70, v191
	v_med3_f32 v139, v139, s70, v191
	v_cvt_pk_fp8_f32 v24, v157, v158 op_sel:[0,0,1]
	v_cvt_pk_fp8_f32 v25, v154, v155 op_sel:[0,0,1]
	v_cvt_pk_fp8_f32 v26, v142, v143 op_sel:[0,0,1]
	v_cvt_pk_fp8_f32 v27, v138, v139 op_sel:[0,0,1]
	v_mul_f32_e32 v176, 0x42800000, v179
	v_pk_fma_f32 v[144:145], v[144:145], s[16:17], v[8:9] op_sel_hi:[1,0,1]
	v_pk_mul_f32 v[148:149], v[148:149], v[176:177] op_sel_hi:[1,0]
	v_pk_mul_f32 v[144:145], v[144:145], v[176:177] op_sel_hi:[1,0]
	v_med3_f32 v148, v148, s70, v191
	v_med3_f32 v144, v144, s70, v191
	v_med3_f32 v149, v149, s70, v191
	v_med3_f32 v21, v145, s70, v191
	global_store_dwordx2 v[16:17], v[24:25], off
	global_store_dwordx2 v[16:17], v[26:27], off offset:128
	v_mov_b32_e32 v24, 0
	v_mov_b32_e32 v25, 0
	v_cvt_pk_fp8_f32 v24, v148, v149
	v_cvt_pk_fp8_f32 v25, v144, v21
	v_pk_fma_f32 v[150:151], v[150:151], s[16:17], v[14:15] op_sel_hi:[1,0,1]
	v_pk_fma_f32 v[146:147], v[146:147], s[16:17], v[10:11] op_sel_hi:[1,0,1]
	v_pk_mul_f32 v[150:151], v[150:151], v[176:177] op_sel_hi:[1,0]
	v_pk_mul_f32 v[146:147], v[146:147], v[176:177] op_sel_hi:[1,0]
	v_pk_fma_f32 v[132:133], v[132:133], s[16:17], v[4:5] op_sel_hi:[1,0,1]
	v_pk_fma_f32 v[128:129], v[128:129], s[16:17], v[0:1] op_sel_hi:[1,0,1]
	v_med3_f32 v136, v150, s70, v191
	v_med3_f32 v26, v146, s70, v191
	v_med3_f32 v21, v151, s70, v191
	v_med3_f32 v27, v147, s70, v191
	v_pk_mul_f32 v[132:133], v[132:133], v[176:177] op_sel_hi:[1,0]
	v_pk_mul_f32 v[128:129], v[128:129], v[176:177] op_sel_hi:[1,0]
	v_cvt_pk_fp8_f32 v24, v136, v21 op_sel:[0,0,1]
	v_cvt_pk_fp8_f32 v25, v26, v27 op_sel:[0,0,1]
	v_pk_fma_f32 v[26:27], v[134:135], s[16:17], v[6:7] op_sel_hi:[1,0,1]
	v_med3_f32 v21, v132, s70, v191
	v_med3_f32 v132, v128, s70, v191
	v_med3_f32 v133, v133, s70, v191
	v_med3_f32 v134, v129, s70, v191
	v_mov_b32_e32 v128, 0
	v_mov_b32_e32 v129, 0
	v_cvt_pk_fp8_f32 v128, v21, v133
	v_cvt_pk_fp8_f32 v129, v132, v134
	v_pk_fma_f32 v[130:131], v[130:131], s[16:17], v[2:3] op_sel_hi:[1,0,1]
	v_pk_mul_f32 v[26:27], v[26:27], v[176:177] op_sel_hi:[1,0]
	v_pk_mul_f32 v[130:131], v[130:131], v[176:177] op_sel_hi:[1,0]
	v_med3_f32 v26, v26, s70, v191
	v_med3_f32 v130, v130, s70, v191
	v_med3_f32 v21, v27, s70, v191
	v_med3_f32 v27, v131, s70, v191
	v_cvt_pk_fp8_f32 v128, v26, v21 op_sel:[0,0,1]
	v_cvt_pk_fp8_f32 v129, v130, v27 op_sel:[0,0,1]
	global_store_dwordx2 v[22:23], v[24:25], off
;     __device__ __forceinline__ void operator()(const f32x4 (&acc)[2][2][4][2], const Unit& u, int wr, int wc, int fr, int fq) const {
;     ...
;         for (int ai = 0; ai < 2; ++ai)
; #pragma unroll
;             for (int m = 0; m < 4; ++m) { const int r = row0 + ai * HALF + m * 16; const float w8 = wq[ai][m] * oscale; unsigned char* rowp = O + (size_t)r * ldc + col0;
; #pragma unroll
;                 for (int bj = 0; bj < 2; ++bj) { f32x4 v0 = (acc[ai][bj][m][0] * ascale + bv[bj][0]) * w8, v1 = (acc[ai][bj][m][1] * ascale + bv[bj][1]) * w8;
; #pragma unroll
;                     for (int j = 0; j < 4; ++j) { v0[j] = __builtin_amdgcn_fmed3f(v0[j], -448.0f, 448.0f); v1[j] = __builtin_amdgcn_fmed3f(v1[j], -448.0f, 448.0f); }
;                     int w0 = 0, w1 = 0;
;                     w0 = __builtin_amdgcn_cvt_pk_fp8_f32(v0[0], v0[1], w0, false); w0 = __builtin_amdgcn_cvt_pk_fp8_f32(v0[2], v0[3], w0, true);
;                     w1 = __builtin_amdgcn_cvt_pk_fp8_f32(v1[0], v1[1], w1, false); w1 = __builtin_amdgcn_cvt_pk_fp8_f32(v1[2], v1[3], w1, true);
;                     u32x2 w; w.x = (unsigned)w0; w.y = (unsigned)w1; *(u32x2*)(rowp + bj * HALF) = w; } }
	global_store_dwordx2 v[22:23], v[128:129], off offset:128
	v_mul_f32_e32 v22, 0x42800000, v175
	v_lshlrev_b64 v[24:25], 11, v[28:29]
	v_pk_fma_f32 v[28:29], v[124:125], s[16:17], v[12:13] op_sel_hi:[1,0,1]
	v_pk_fma_f32 v[120:121], v[120:121], s[16:17], v[8:9] op_sel_hi:[1,0,1]
	v_pk_mul_f32 v[28:29], v[28:29], v[22:23] op_sel_hi:[1,0]
	v_pk_fma_f32 v[26:27], v[126:127], s[16:17], v[14:15] op_sel_hi:[1,0,1]
	v_pk_fma_f32 v[122:123], v[122:123], s[16:17], v[10:11] op_sel_hi:[1,0,1]
	v_pk_mul_f32 v[120:121], v[120:121], v[22:23] op_sel_hi:[1,0]
	v_med3_f32 v21, v28, s70, v191
	v_med3_f32 v29, v29, s70, v191
	v_mov_b32_e32 v28, 0
	v_pk_mul_f32 v[26:27], v[26:27], v[22:23] op_sel_hi:[1,0]
	v_pk_mul_f32 v[122:123], v[122:123], v[22:23] op_sel_hi:[1,0]
	v_med3_f32 v23, v120, s70, v191
	v_med3_f32 v120, v121, s70, v191
	v_cvt_pk_fp8_f32 v28, v21, v29
	v_mov_b32_e32 v29, 0
	v_cvt_pk_fp8_f32 v29, v23, v120
	v_med3_f32 v26, v26, s70, v191
	v_med3_f32 v21, v27, s70, v191
	v_med3_f32 v121, v122, s70, v191
	v_med3_f32 v23, v123, s70, v191
	v_cvt_pk_fp8_f32 v28, v26, v21 op_sel:[0,0,1]
	v_pk_fma_f32 v[26:27], v[118:119], s[16:17], v[6:7] op_sel_hi:[1,0,1]
	v_pk_fma_f32 v[116:117], v[116:117], s[16:17], v[4:5] op_sel_hi:[1,0,1]
	v_pk_fma_f32 v[114:115], v[114:115], s[16:17], v[2:3] op_sel_hi:[1,0,1]
	v_pk_fma_f32 v[112:113], v[112:113], s[16:17], v[0:1] op_sel_hi:[1,0,1]
	v_cvt_pk_fp8_f32 v29, v121, v23 op_sel:[0,0,1]
	v_pk_mul_f32 v[26:27], v[26:27], v[22:23] op_sel_hi:[1,0]
	v_pk_mul_f32 v[116:117], v[116:117], v[22:23] op_sel_hi:[1,0]
	v_pk_mul_f32 v[114:115], v[114:115], v[22:23] op_sel_hi:[1,0]
	v_pk_mul_f32 v[22:23], v[112:113], v[22:23] op_sel_hi:[1,0]
	v_med3_f32 v21, v116, s70, v191
	v_med3_f32 v112, v22, s70, v191
	v_med3_f32 v113, v117, s70, v191
	v_med3_f32 v116, v23, s70, v191
	v_mov_b32_e32 v22, 0
	v_mov_b32_e32 v23, 0
	v_cvt_pk_fp8_f32 v22, v21, v113
	v_cvt_pk_fp8_f32 v23, v112, v116
	v_med3_f32 v26, v26, s70, v191
	v_med3_f32 v114, v114, s70, v191
	v_med3_f32 v21, v27, s70, v191
	v_med3_f32 v27, v115, s70, v191
	v_cvt_pk_fp8_f32 v22, v26, v21 op_sel:[0,0,1]
	v_cvt_pk_fp8_f32 v23, v114, v27 op_sel:[0,0,1]
	v_lshl_add_u64 v[24:25], s[8:9], 0, v[24:25]
	v_lshl_add_u64 v[24:25], v[24:25], 0, v[18:19]
	global_store_dwordx2 v[24:25], v[28:29], off
	global_store_dwordx2 v[24:25], v[22:23], off offset:128
	v_mul_f32_e32 v22, 0x42800000, v177
	v_pk_fma_f32 v[28:29], v[108:109], s[16:17], v[12:13] op_sel_hi:[1,0,1]
	v_pk_fma_f32 v[104:105], v[104:105], s[16:17], v[8:9] op_sel_hi:[1,0,1]
	v_pk_mul_f32 v[28:29], v[28:29], v[22:23] op_sel_hi:[1,0]
	v_lshlrev_b64 v[24:25], 11, v[30:31]
	v_pk_fma_f32 v[26:27], v[110:111], s[16:17], v[14:15] op_sel_hi:[1,0,1]
	v_pk_fma_f32 v[30:31], v[106:107], s[16:17], v[10:11] op_sel_hi:[1,0,1]
	v_pk_mul_f32 v[104:105], v[104:105], v[22:23] op_sel_hi:[1,0]
	v_med3_f32 v21, v28, s70, v191
	v_med3_f32 v29, v29, s70, v191
	v_mov_b32_e32 v28, 0
	v_pk_mul_f32 v[26:27], v[26:27], v[22:23] op_sel_hi:[1,0]
	v_pk_mul_f32 v[30:31], v[30:31], v[22:23] op_sel_hi:[1,0]
	v_med3_f32 v23, v104, s70, v191
	v_med3_f32 v104, v105, s70, v191
	v_cvt_pk_fp8_f32 v28, v21, v29
	v_mov_b32_e32 v29, 0
	v_cvt_pk_fp8_f32 v29, v23, v104
	v_med3_f32 v26, v26, s70, v191
	v_med3_f32 v30, v30, s70, v191
	v_med3_f32 v21, v27, s70, v191
	v_med3_f32 v23, v31, s70, v191
	v_cvt_pk_fp8_f32 v28, v26, v21 op_sel:[0,0,1]
	v_cvt_pk_fp8_f32 v29, v30, v23 op_sel:[0,0,1]
	v_pk_fma_f32 v[26:27], v[102:103], s[16:17], v[6:7] op_sel_hi:[1,0,1]
	v_pk_fma_f32 v[30:31], v[100:101], s[16:17], v[4:5] op_sel_hi:[1,0,1]
	v_pk_fma_f32 v[98:99], v[98:99], s[16:17], v[2:3] op_sel_hi:[1,0,1]
	v_pk_fma_f32 v[96:97], v[96:97], s[16:17], v[0:1] op_sel_hi:[1,0,1]
	v_pk_mul_f32 v[26:27], v[26:27], v[22:23] op_sel_hi:[1,0]
	v_pk_mul_f32 v[30:31], v[30:31], v[22:23] op_sel_hi:[1,0]
	v_pk_mul_f32 v[98:99], v[98:99], v[22:23] op_sel_hi:[1,0]
	v_pk_mul_f32 v[22:23], v[96:97], v[22:23] op_sel_hi:[1,0]
	v_med3_f32 v21, v30, s70, v191
	v_med3_f32 v30, v22, s70, v191
	v_med3_f32 v31, v31, s70, v191
	v_med3_f32 v96, v23, s70, v191
	v_mov_b32_e32 v22, 0
	v_mov_b32_e32 v23, 0
	v_cvt_pk_fp8_f32 v22, v21, v31
	v_cvt_pk_fp8_f32 v23, v30, v96
	v_med3_f32 v26, v26, s70, v191
	v_med3_f32 v97, v98, s70, v191
	v_med3_f32 v21, v27, s70, v191
	v_med3_f32 v27, v99, s70, v191
	v_cvt_pk_fp8_f32 v22, v26, v21 op_sel:[0,0,1]
	v_cvt_pk_fp8_f32 v23, v97, v27 op_sel:[0,0,1]
	v_lshl_add_u64 v[24:25], s[8:9], 0, v[24:25]
	v_lshl_add_u64 v[18:19], v[24:25], 0, v[18:19]
	global_store_dwordx2 v[18:19], v[28:29], off
	global_store_dwordx2 v[18:19], v[22:23], off offset:128
	v_mul_f32_e32 v18, 0x42800000, v180
	v_pk_fma_f32 v[26:27], v[92:93], s[16:17], v[12:13] op_sel_hi:[1,0,1]
	v_pk_fma_f32 v[24:25], v[94:95], s[16:17], v[14:15] op_sel_hi:[1,0,1]
	v_pk_mul_f32 v[26:27], v[26:27], v[18:19] op_sel_hi:[1,0]
	v_pk_fma_f32 v[28:29], v[90:91], s[16:17], v[10:11] op_sel_hi:[1,0,1]
	v_pk_fma_f32 v[30:31], v[88:89], s[16:17], v[8:9] op_sel_hi:[1,0,1]
	v_pk_mul_f32 v[24:25], v[24:25], v[18:19] op_sel_hi:[1,0]
	v_pk_mul_f32 v[28:29], v[28:29], v[18:19] op_sel_hi:[1,0]
	v_pk_mul_f32 v[30:31], v[30:31], v[18:19] op_sel_hi:[1,0]
	v_med3_f32 v19, v26, s70, v191
	v_med3_f32 v27, v27, s70, v191
	v_mov_b32_e32 v26, 0
	v_med3_f32 v21, v30, s70, v191
	v_med3_f32 v30, v31, s70, v191
	v_cvt_pk_fp8_f32 v26, v19, v27
	v_mov_b32_e32 v27, 0
	v_cvt_pk_fp8_f32 v27, v21, v30
	v_med3_f32 v24, v24, s70, v191
	v_med3_f32 v28, v28, s70, v191
	v_med3_f32 v19, v25, s70, v191
	v_med3_f32 v21, v29, s70, v191
	v_cvt_pk_fp8_f32 v26, v24, v19 op_sel:[0,0,1]
	v_cvt_pk_fp8_f32 v27, v28, v21 op_sel:[0,0,1]
	v_pk_fma_f32 v[24:25], v[86:87], s[16:17], v[6:7] op_sel_hi:[1,0,1]
;     __device__ __forceinline__ void operator()(const f32x4 (&acc)[2][2][4][2], const Unit& u, int wr, int wc, int fr, int fq) const {
;     ...
;         for (int ai = 0; ai < 2; ++ai)
; #pragma unroll
;             for (int m = 0; m < 4; ++m) { const int r = row0 + ai * HALF + m * 16; const float w8 = wq[ai][m] * oscale; unsigned char* rowp = O + (size_t)r * ldc + col0;
; #pragma unroll
;                 for (int bj = 0; bj < 2; ++bj) { f32x4 v0 = (acc[ai][bj][m][0] * ascale + bv[bj][0]) * w8, v1 = (acc[ai][bj][m][1] * ascale + bv[bj][1]) * w8;
; #pragma unroll
;                     for (int j = 0; j < 4; ++j) { v0[j] = __builtin_amdgcn_fmed3f(v0[j], -448.0f, 448.0f); v1[j] = __builtin_amdgcn_fmed3f(v1[j], -448.0f, 448.0f); }
;                     int w0 = 0, w1 = 0;
;                     w0 = __builtin_amdgcn_cvt_pk_fp8_f32(v0[0], v0[1], w0, false); w0 = __builtin_amdgcn_cvt_pk_fp8_f32(v0[2], v0[3], w0, true);
;                     w1 = __builtin_amdgcn_cvt_pk_fp8_f32(v1[0], v1[1], w1, false); w1 = __builtin_amdgcn_cvt_pk_fp8_f32(v1[2], v1[3], w1, true);
;                     u32x2 w; w.x = (unsigned)w0; w.y = (unsigned)w1; *(u32x2*)(rowp + bj * HALF) = w; } }
	v_pk_fma_f32 v[28:29], v[84:85], s[16:17], v[4:5] op_sel_hi:[1,0,1]
	v_pk_fma_f32 v[30:31], v[82:83], s[16:17], v[2:3] op_sel_hi:[1,0,1]
	v_pk_fma_f32 v[80:81], v[80:81], s[16:17], v[0:1] op_sel_hi:[1,0,1]
	v_pk_mul_f32 v[24:25], v[24:25], v[18:19] op_sel_hi:[1,0]
	v_pk_mul_f32 v[28:29], v[28:29], v[18:19] op_sel_hi:[1,0]
	v_pk_mul_f32 v[30:31], v[30:31], v[18:19] op_sel_hi:[1,0]
	v_pk_mul_f32 v[18:19], v[80:81], v[18:19] op_sel_hi:[1,0]
	v_med3_f32 v21, v28, s70, v191
	v_med3_f32 v28, v18, s70, v191
	v_med3_f32 v29, v29, s70, v191
	v_med3_f32 v80, v19, s70, v191
	v_mov_b32_e32 v18, 0
	v_mov_b32_e32 v19, 0
	v_cvt_pk_fp8_f32 v18, v21, v29
	v_cvt_pk_fp8_f32 v19, v28, v80
	v_med3_f32 v24, v24, s70, v191
	v_med3_f32 v30, v30, s70, v191
	v_med3_f32 v21, v25, s70, v191
	v_med3_f32 v25, v31, s70, v191
	v_cvt_pk_fp8_f32 v18, v24, v21 op_sel:[0,0,1]
	v_cvt_pk_fp8_f32 v19, v30, v25 op_sel:[0,0,1]
	v_add_co_u32_e32 v24, vcc, s71, v16
	v_lshl_add_u64 v[22:23], v[16:17], 0, s[4:5]
	s_nop 0
	v_addc_co_u32_e32 v25, vcc, 0, v17, vcc
	global_store_dwordx2 v[24:25], v[26:27], off
	global_store_dwordx2 v[22:23], v[18:19], off offset:128
	v_mul_f32_e32 v18, 0x42800000, v181
	v_pk_fma_f32 v[26:27], v[76:77], s[16:17], v[12:13] op_sel_hi:[1,0,1]
	v_pk_fma_f32 v[24:25], v[78:79], s[16:17], v[14:15] op_sel_hi:[1,0,1]
	v_pk_mul_f32 v[26:27], v[26:27], v[18:19] op_sel_hi:[1,0]
	v_pk_fma_f32 v[28:29], v[74:75], s[16:17], v[10:11] op_sel_hi:[1,0,1]
	v_pk_fma_f32 v[30:31], v[72:73], s[16:17], v[8:9] op_sel_hi:[1,0,1]
	v_pk_mul_f32 v[24:25], v[24:25], v[18:19] op_sel_hi:[1,0]
	v_pk_mul_f32 v[28:29], v[28:29], v[18:19] op_sel_hi:[1,0]
	v_pk_mul_f32 v[30:31], v[30:31], v[18:19] op_sel_hi:[1,0]
	v_med3_f32 v19, v26, s70, v191
	v_med3_f32 v27, v27, s70, v191
	v_mov_b32_e32 v26, 0
	v_med3_f32 v21, v30, s70, v191
	v_med3_f32 v30, v31, s70, v191
	v_cvt_pk_fp8_f32 v26, v19, v27
	v_mov_b32_e32 v27, 0
	v_cvt_pk_fp8_f32 v27, v21, v30
	v_med3_f32 v24, v24, s70, v191
	v_med3_f32 v28, v28, s70, v191
	v_med3_f32 v19, v25, s70, v191
	v_med3_f32 v21, v29, s70, v191
	v_cvt_pk_fp8_f32 v26, v24, v19 op_sel:[0,0,1]
	v_cvt_pk_fp8_f32 v27, v28, v21 op_sel:[0,0,1]
	v_pk_fma_f32 v[24:25], v[70:71], s[16:17], v[6:7] op_sel_hi:[1,0,1]
	v_pk_fma_f32 v[28:29], v[68:69], s[16:17], v[4:5] op_sel_hi:[1,0,1]
	v_pk_fma_f32 v[30:31], v[66:67], s[16:17], v[2:3] op_sel_hi:[1,0,1]
	v_pk_fma_f32 v[64:65], v[64:65], s[16:17], v[0:1] op_sel_hi:[1,0,1]
	v_pk_mul_f32 v[24:25], v[24:25], v[18:19] op_sel_hi:[1,0]
	v_pk_mul_f32 v[28:29], v[28:29], v[18:19] op_sel_hi:[1,0]
	v_pk_mul_f32 v[30:31], v[30:31], v[18:19] op_sel_hi:[1,0]
	v_pk_mul_f32 v[18:19], v[64:65], v[18:19] op_sel_hi:[1,0]
	v_med3_f32 v21, v28, s70, v191
	v_med3_f32 v28, v18, s70, v191
	v_med3_f32 v29, v29, s70, v191
	v_med3_f32 v64, v19, s70, v191
	v_mov_b32_e32 v18, 0
	v_mov_b32_e32 v19, 0
	v_cvt_pk_fp8_f32 v18, v21, v29
	v_cvt_pk_fp8_f32 v19, v28, v64
	v_med3_f32 v24, v24, s70, v191
	v_med3_f32 v30, v30, s70, v191
	v_med3_f32 v21, v25, s70, v191
	v_med3_f32 v25, v31, s70, v191
	v_cvt_pk_fp8_f32 v18, v24, v21 op_sel:[0,0,1]
	v_cvt_pk_fp8_f32 v19, v30, v25 op_sel:[0,0,1]
	v_add_co_u32_e32 v24, vcc, s72, v16
	v_lshl_add_u64 v[22:23], v[16:17], 0, s[18:19]
	s_nop 0
	v_addc_co_u32_e32 v25, vcc, 0, v17, vcc
	global_store_dwordx2 v[24:25], v[26:27], off
	global_store_dwordx2 v[22:23], v[18:19], off offset:128
	v_mul_f32_e32 v18, 0x42800000, v182
	v_pk_fma_f32 v[26:27], v[60:61], s[16:17], v[12:13] op_sel_hi:[1,0,1]
	v_pk_fma_f32 v[24:25], v[62:63], s[16:17], v[14:15] op_sel_hi:[1,0,1]
	v_pk_mul_f32 v[26:27], v[26:27], v[18:19] op_sel_hi:[1,0]
	v_pk_fma_f32 v[28:29], v[58:59], s[16:17], v[10:11] op_sel_hi:[1,0,1]
	v_pk_fma_f32 v[30:31], v[56:57], s[16:17], v[8:9] op_sel_hi:[1,0,1]
	v_pk_mul_f32 v[24:25], v[24:25], v[18:19] op_sel_hi:[1,0]
	v_pk_mul_f32 v[28:29], v[28:29], v[18:19] op_sel_hi:[1,0]
	v_pk_mul_f32 v[30:31], v[30:31], v[18:19] op_sel_hi:[1,0]
	v_med3_f32 v19, v26, s70, v191
; #define PG8_BAR __builtin_amdgcn_s_barrier()
;     __device__ __forceinline__ void operator()(const f32x4 (&acc)[2][2][4][2], const Unit& u, int wr, int wc, int fr, int fq) const {
;     ...
;         for (int ai = 0; ai < 2; ++ai)
; #pragma unroll
;             for (int m = 0; m < 4; ++m) { const int r = row0 + ai * HALF + m * 16; const float w8 = wq[ai][m] * oscale; unsigned char* rowp = O + (size_t)r * ldc + col0;
; #pragma unroll
;                 for (int bj = 0; bj < 2; ++bj) { f32x4 v0 = (acc[ai][bj][m][0] * ascale + bv[bj][0]) * w8, v1 = (acc[ai][bj][m][1] * ascale + bv[bj][1]) * w8;
; #pragma unroll
;                     for (int j = 0; j < 4; ++j) { v0[j] = __builtin_amdgcn_fmed3f(v0[j], -448.0f, 448.0f); v1[j] = __builtin_amdgcn_fmed3f(v1[j], -448.0f, 448.0f); }
;                     int w0 = 0, w1 = 0;
;                     w0 = __builtin_amdgcn_cvt_pk_fp8_f32(v0[0], v0[1], w0, false); w0 = __builtin_amdgcn_cvt_pk_fp8_f32(v0[2], v0[3], w0, true);
;                     w1 = __builtin_amdgcn_cvt_pk_fp8_f32(v1[0], v1[1], w1, false); w1 = __builtin_amdgcn_cvt_pk_fp8_f32(v1[2], v1[3], w1, true);
;                     u32x2 w; w.x = (unsigned)w0; w.y = (unsigned)w1; *(u32x2*)(rowp + bj * HALF) = w; } }
; template <class Epi, class Sched, bool ALIGN_EPI = false, bool SP2 = false, bool GATHER = false, bool F8 = false>
; __device__ __forceinline__ void gemm_phase(PG8_LAS unsigned char* lds, const Gemm g, const Sched& S, const Epi& E) {
;     ...
;         if (!has_next) break;
;         if (!(Epi::MID && cur.kh == 0)) {
; #pragma unroll
;         for (int a = 0; a < 2; ++a)
; #pragma unroll
;             for (int b = 0; b < 2; ++b)
; #pragma unroll
;                 for (int m = 0; m < 4; ++m)
; #pragma unroll
;                     for (int n = 0; n < 2; ++n) acc[a][b][m][n] = (f32x4){0.f, 0.f, 0.f, 0.f}; }
;         cur = nxt; cA = nA; cB = nB; ++ui;
;         if constexpr (GATHER) { gc0[0] = gn0[0]; gc0[1] = gn0[1]; gc1[0] = gn1[0]; gc1[1] = gn1[1]; }
;         if constexpr (ALIGN_EPI) { if (wr == 1) PG8_BAR; }
	v_med3_f32 v27, v27, s70, v191
	v_mov_b32_e32 v26, 0
	v_med3_f32 v21, v30, s70, v191
	v_med3_f32 v30, v31, s70, v191
	v_cvt_pk_fp8_f32 v26, v19, v27
	v_mov_b32_e32 v27, 0
	v_cvt_pk_fp8_f32 v27, v21, v30
	v_med3_f32 v24, v24, s70, v191
	v_med3_f32 v28, v28, s70, v191
	v_med3_f32 v19, v25, s70, v191
	v_med3_f32 v21, v29, s70, v191
	v_cvt_pk_fp8_f32 v26, v24, v19 op_sel:[0,0,1]
	v_cvt_pk_fp8_f32 v27, v28, v21 op_sel:[0,0,1]
	v_pk_fma_f32 v[24:25], v[54:55], s[16:17], v[6:7] op_sel_hi:[1,0,1]
	v_pk_fma_f32 v[28:29], v[52:53], s[16:17], v[4:5] op_sel_hi:[1,0,1]
	v_pk_fma_f32 v[30:31], v[50:51], s[16:17], v[2:3] op_sel_hi:[1,0,1]
	v_pk_fma_f32 v[48:49], v[48:49], s[16:17], v[0:1] op_sel_hi:[1,0,1]
	v_pk_mul_f32 v[24:25], v[24:25], v[18:19] op_sel_hi:[1,0]
	v_pk_mul_f32 v[28:29], v[28:29], v[18:19] op_sel_hi:[1,0]
	v_pk_mul_f32 v[30:31], v[30:31], v[18:19] op_sel_hi:[1,0]
	v_pk_mul_f32 v[18:19], v[48:49], v[18:19] op_sel_hi:[1,0]
	v_med3_f32 v21, v28, s70, v191
	v_med3_f32 v28, v18, s70, v191
	v_med3_f32 v29, v29, s70, v191
	v_med3_f32 v48, v19, s70, v191
	v_mov_b32_e32 v18, 0
	v_mov_b32_e32 v19, 0
	v_cvt_pk_fp8_f32 v18, v21, v29
	v_cvt_pk_fp8_f32 v19, v28, v48
	v_med3_f32 v24, v24, s70, v191
	v_med3_f32 v30, v30, s70, v191
	v_med3_f32 v21, v25, s70, v191
	v_med3_f32 v25, v31, s70, v191
	v_cvt_pk_fp8_f32 v18, v24, v21 op_sel:[0,0,1]
	v_cvt_pk_fp8_f32 v19, v30, v25 op_sel:[0,0,1]
	v_add_co_u32_e32 v24, vcc, s73, v16
	v_lshl_add_u64 v[22:23], v[16:17], 0, s[22:23]
	s_nop 0
	v_addc_co_u32_e32 v25, vcc, 0, v17, vcc
	global_store_dwordx2 v[24:25], v[26:27], off
	global_store_dwordx2 v[22:23], v[18:19], off offset:128
	v_mul_f32_e32 v18, 0x42800000, v20
	v_pk_fma_f32 v[8:9], v[40:41], s[16:17], v[8:9] op_sel_hi:[1,0,1]
	v_pk_fma_f32 v[14:15], v[46:47], s[16:17], v[14:15] op_sel_hi:[1,0,1]
	v_pk_fma_f32 v[12:13], v[44:45], s[16:17], v[12:13] op_sel_hi:[1,0,1]
	v_pk_fma_f32 v[10:11], v[42:43], s[16:17], v[10:11] op_sel_hi:[1,0,1]
	v_pk_mul_f32 v[8:9], v[8:9], v[18:19] op_sel_hi:[1,0]
	v_pk_mul_f32 v[14:15], v[14:15], v[18:19] op_sel_hi:[1,0]
	v_pk_mul_f32 v[12:13], v[12:13], v[18:19] op_sel_hi:[1,0]
	v_pk_mul_f32 v[10:11], v[10:11], v[18:19] op_sel_hi:[1,0]
	v_med3_f32 v19, v8, s70, v191
	v_med3_f32 v22, v9, s70, v191
	v_mov_b32_e32 v9, 0
	v_cvt_pk_fp8_f32 v9, v19, v22
	v_pk_fma_f32 v[4:5], v[36:37], s[16:17], v[4:5] op_sel_hi:[1,0,1]
	v_pk_fma_f32 v[0:1], v[32:33], s[16:17], v[0:1] op_sel_hi:[1,0,1]
	v_med3_f32 v12, v12, s70, v191
	v_med3_f32 v13, v13, s70, v191
	v_med3_f32 v10, v10, s70, v191
	v_mov_b32_e32 v8, 0
	v_med3_f32 v11, v11, s70, v191
	v_pk_mul_f32 v[4:5], v[4:5], v[18:19] op_sel_hi:[1,0]
	v_pk_mul_f32 v[0:1], v[0:1], v[18:19] op_sel_hi:[1,0]
	v_cvt_pk_fp8_f32 v8, v12, v13
	v_cvt_pk_fp8_f32 v9, v10, v11 op_sel:[0,0,1]
	v_med3_f32 v4, v4, s70, v191
	v_med3_f32 v10, v0, s70, v191
	v_med3_f32 v5, v5, s70, v191
	v_med3_f32 v11, v1, s70, v191
	v_mov_b32_e32 v0, 0
	v_mov_b32_e32 v1, 0
	v_cvt_pk_fp8_f32 v0, v4, v5
	v_cvt_pk_fp8_f32 v1, v10, v11
	v_pk_fma_f32 v[6:7], v[38:39], s[16:17], v[6:7] op_sel_hi:[1,0,1]
	v_pk_fma_f32 v[2:3], v[34:35], s[16:17], v[2:3] op_sel_hi:[1,0,1]
	v_med3_f32 v14, v14, s70, v191
	v_med3_f32 v12, v15, s70, v191
	v_pk_mul_f32 v[6:7], v[6:7], v[18:19] op_sel_hi:[1,0]
	v_pk_mul_f32 v[2:3], v[2:3], v[18:19] op_sel_hi:[1,0]
	v_cvt_pk_fp8_f32 v8, v14, v12 op_sel:[0,0,1]
	v_med3_f32 v6, v6, s70, v191
	v_med3_f32 v2, v2, s70, v191
	v_med3_f32 v4, v7, s70, v191
	v_med3_f32 v3, v3, s70, v191
	v_cvt_pk_fp8_f32 v0, v6, v4 op_sel:[0,0,1]
	v_cvt_pk_fp8_f32 v1, v2, v3 op_sel:[0,0,1]
	v_add_co_u32_e32 v2, vcc, s74, v16
	v_lshl_add_u64 v[20:21], v[16:17], 0, s[34:35]
	s_nop 0
	v_addc_co_u32_e32 v3, vcc, 0, v17, vcc
	s_andn2_b64 vcc, exec, s[0:1]
	s_mov_b64 s[0:1], -1
	global_store_dwordx2 v[2:3], v[8:9], off
	global_store_dwordx2 v[20:21], v[0:1], off offset:128
	s_cbranch_vccnz .LBB0_1559
	s_andn2_b64 vcc, exec, s[6:7]
	s_cbranch_vccnz .LBB0_1558
	s_barrier
	s_branch .LBB0_1558
